# speedup vs baseline: 1.0059x; 1.0059x over previous
_Z11edge_kernelILi36ELb1EEvPKfS1_PKDF16_PKiS5_S1_S1_S1_S1_S1_PDF16_:
	s_load_dwordx8 s[4:11], s[0:1], 0x0
	s_load_dwordx8 s[12:19], s[0:1], 0x20
	s_load_dwordx4 s[20:23], s[0:1], 0x40
	s_load_dwordx2 s[24:25], s[0:1], 0x50
	v_readfirstlane_b32 s3, v0
	v_bfe_u32 v75, v0, 4, 2
	v_and_b32_e32 v76, 15, v0
	v_and_b32_e32 v78, 63, v0
	s_lshr_b32 s3, s3, 6
	s_mul_i32 s26, s3, 0x1388
	s_add_i32 s2, s2, s26
	v_lshlrev_b32_e32 v74, 8, v75
	v_lshl_or_b32 v74, v76, 4, v74
	v_lshlrev_b32_e32 v79, 4, v78
	v_lshl_or_b32 v77, v76, 2, v75
	v_lshlrev_b32_e32 v77, 2, v77
	v_mul_u32_u24_e32 v73, 0x900, v75
	v_lshl_or_b32 v73, v76, 4, v73
	v_mul_u32_u24_e32 v78, 36, v75
	s_mul_i32 s28, s2, 0x2400
	s_lshl_b32 s29, s2, 14
	s_lshl_b32 s30, s2, 2
	s_lshl_b32 s31, s2, 8
	s_lshl_b32 s33, s3, 10
	s_lshl_b32 s34, s3, 8
	s_addk_i32 s34, 0x4000
	s_waitcnt lgkmcnt(0)
	s_add_u32 s10, s10, s30
	s_addc_u32 s11, s11, 0
	s_add_u32 s12, s12, s30
	s_addc_u32 s13, s13, 0
	s_load_dword s35, s[10:11], 0x0
	s_load_dword s36, s[12:13], 0x0
	s_add_u32 s14, s14, s28
	s_addc_u32 s15, s15, 0
	global_load_dwordx4 v[0:3], v73, s[14:15] nt
	global_load_dwordx4 v[4:7], v73, s[14:15] offset:256 nt
	global_load_dwordx4 v[8:11], v73, s[14:15] offset:512 nt
	global_load_dwordx4 v[12:15], v73, s[14:15] offset:768 nt
	global_load_dwordx4 v[16:19], v73, s[14:15] offset:1024 nt
	global_load_dwordx4 v[20:23], v73, s[14:15] offset:1280 nt
	global_load_dwordx4 v[24:27], v73, s[14:15] offset:1536 nt
	global_load_dwordx4 v[28:31], v73, s[14:15] offset:1792 nt
	global_load_dwordx4 v[32:35], v73, s[14:15] offset:2048 nt
	s_add_u32 s22, s22, s33
	s_addc_u32 s23, s23, 0
	s_add_u32 s18, s18, s29
	s_addc_u32 s19, s19, 0
	s_add_u32 s16, s16, s31
	s_addc_u32 s17, s17, 0
	s_add_u32 s20, s20, s31
	s_addc_u32 s21, s21, 0
	s_waitcnt lgkmcnt(0)
	s_lshl_b32 s36, s36, 7
	s_add_u32 s24, s24, s36
	s_addc_u32 s25, s25, 0
	s_lshl_b32 s37, s35, 7
	s_lshl_b32 s38, s35, 4
	s_add_u32 s4, s4, s37
	s_addc_u32 s5, s5, 0
	s_add_u32 s6, s6, s38
	s_addc_u32 s7, s7, 0
	v_mov_b32_e32 v93, 0
	v_mov_b32_e32 v92, v78
	v_lshl_add_u64 v[94:95], s[4:5], 0, v[92:93]
	v_lshl_add_u64 v[94:95], v[94:95], 0, 20
	v_cmp_eq_u32_e32 vcc, 3, v75
	s_nop 1
	v_mov_b32_e32 v90, s6
	v_mov_b32_e32 v91, s7
	v_cndmask_b32_e32 v94, v94, v90, vcc
	v_cndmask_b32_e32 v95, v95, v91, vcc
	global_load_dwordx4 v[80:83], v78, s[4:5] nt
	global_load_dword v84, v78, s[4:5] offset:16 nt
	global_load_dwordx4 v[86:89], v[94:95], off nt
	global_load_dword v72, v77, s[16:17] nt
	global_load_dword v64, v77, s[20:21] nt
	s_mov_b32 m0, s33
	s_nop 0
	global_load_lds_dwordx4 v79, s[22:23]
	global_load_lds_dwordx4 v79, s[22:23] offset:2048
	s_add_u32 m0, m0, 0x1000
	s_add_u32 s22, s22, 0x1000
	s_addc_u32 s23, s23, 0
	global_load_lds_dwordx4 v79, s[22:23]
	global_load_lds_dwordx4 v79, s[22:23] offset:2048
	s_add_u32 m0, m0, 0x1000
	s_add_u32 s22, s22, 0x1000
	s_addc_u32 s23, s23, 0
	global_load_lds_dwordx4 v79, s[22:23]
	global_load_lds_dwordx4 v79, s[22:23] offset:2048
	s_add_u32 m0, m0, 0x1000
	s_add_u32 s22, s22, 0x1000
	s_addc_u32 s23, s23, 0
	global_load_lds_dwordx4 v79, s[22:23]
	global_load_lds_dwordx4 v79, s[22:23] offset:2048
	v_add_u32_e32 v78, s34, v77
	v_lshl_add_u32 v79, v75, 2, s34
	s_waitcnt vmcnt(10)
	v_pk_mul_f32 v[96:97], v[80:81], v[0:1] op_sel_hi:[0,1]
	v_pk_mul_f32 v[98:99], v[80:81], v[2:3] op_sel_hi:[0,1]
	v_pk_mul_f32 v[100:101], v[80:81], v[4:5] op_sel:[1,0]
	v_pk_mul_f32 v[102:103], v[80:81], v[6:7] op_sel:[1,0]
	v_pk_fma_f32 v[96:97], v[82:83], v[8:9], v[96:97] op_sel_hi:[0,1,1]
	v_pk_fma_f32 v[98:99], v[82:83], v[10:11], v[98:99] op_sel_hi:[0,1,1]
	v_pk_fma_f32 v[100:101], v[82:83], v[12:13], v[100:101] op_sel:[1,0,0]
	v_pk_fma_f32 v[102:103], v[82:83], v[14:15], v[102:103] op_sel:[1,0,0]
	v_pk_fma_f32 v[96:97], v[84:85], v[16:17], v[96:97] op_sel_hi:[0,1,1]
	v_pk_fma_f32 v[98:99], v[84:85], v[18:19], v[98:99] op_sel_hi:[0,1,1]
	v_pk_fma_f32 v[100:101], v[86:87], v[20:21], v[100:101] op_sel_hi:[0,1,1]
	v_pk_fma_f32 v[102:103], v[86:87], v[22:23], v[102:103] op_sel_hi:[0,1,1]
	v_pk_fma_f32 v[96:97], v[86:87], v[24:25], v[96:97] op_sel:[1,0,0]
	v_pk_fma_f32 v[98:99], v[86:87], v[26:27], v[98:99] op_sel:[1,0,0]
	v_pk_fma_f32 v[100:101], v[88:89], v[28:29], v[100:101] op_sel_hi:[0,1,1]
	v_pk_fma_f32 v[102:103], v[88:89], v[30:31], v[102:103] op_sel_hi:[0,1,1]
	v_pk_fma_f32 v[96:97], v[88:89], v[32:33], v[96:97] op_sel:[1,0,0]
	v_pk_fma_f32 v[98:99], v[88:89], v[34:35], v[98:99] op_sel:[1,0,0]
	v_pk_add_f32 v[96:97], v[96:97], v[100:101]
	v_pk_add_f32 v[98:99], v[98:99], v[102:103]
	s_nop 1
	v_permlane16_swap_b32_e32 v96, v97
	v_permlane16_swap_b32_e32 v98, v99
	v_add_f32_e32 v96, v96, v97
	v_add_f32_e32 v98, v98, v99
	s_nop 1
	v_permlane32_swap_b32_e32 v96, v98
	v_add_f32_e32 v96, v96, v98
	s_waitcnt vmcnt(9)
	v_add_f32_e32 v96, v96, v72
	v_max_f32_e32 v96, 0, v96
	ds_write_b32 v78, v96
	ds_read2_b32 v[80:81], v79 offset0:0 offset1:4
	ds_read2_b32 v[82:83], v79 offset0:8 offset1:12
	ds_read2_b32 v[84:85], v79 offset0:16 offset1:20
	ds_read2_b32 v[86:87], v79 offset0:24 offset1:28
	ds_read2_b32 v[88:89], v79 offset0:32 offset1:36
	ds_read2_b32 v[90:91], v79 offset0:40 offset1:44
	ds_read2_b32 v[92:93], v79 offset0:48 offset1:52
	ds_read2_b32 v[94:95], v79 offset0:56 offset1:60
	s_waitcnt lgkmcnt(0)
	v_cmp_neq_f32_e64 s[40:41], 0, v80
	v_cmp_neq_f32_e64 s[42:43], 0, v81
	v_cmp_neq_f32_e64 s[44:45], 0, v82
	v_cmp_neq_f32_e64 s[46:47], 0, v83
	v_cmp_neq_f32_e64 s[48:49], 0, v84
	v_cmp_neq_f32_e64 s[50:51], 0, v85
	v_cmp_neq_f32_e64 s[52:53], 0, v86
	v_cmp_neq_f32_e64 s[54:55], 0, v87
	v_cmp_neq_f32_e64 s[56:57], 0, v88
	v_cmp_neq_f32_e64 s[58:59], 0, v89
	v_cmp_neq_f32_e64 s[60:61], 0, v90
	v_cmp_neq_f32_e64 s[62:63], 0, v91
	v_cmp_neq_f32_e64 s[64:65], 0, v92
	v_cmp_neq_f32_e64 s[66:67], 0, v93
	v_cmp_neq_f32_e64 s[68:69], 0, v94
	v_cmp_neq_f32_e64 s[70:71], 0, v95
	s_mov_b64 exec, s[40:41]
	global_load_dwordx4 v[0:3], v74, s[18:19] nt
	s_mov_b64 exec, s[42:43]
	global_load_dwordx4 v[4:7], v74, s[18:19] offset:1024 nt
	s_mov_b64 exec, s[44:45]
	global_load_dwordx4 v[8:11], v74, s[18:19] offset:2048 nt
	s_mov_b64 exec, s[46:47]
	global_load_dwordx4 v[12:15], v74, s[18:19] offset:3072 nt
	s_add_u32 s18, s18, 0x1000
	s_addc_u32 s19, s19, 0
	s_mov_b64 exec, s[48:49]
	global_load_dwordx4 v[16:19], v74, s[18:19] nt
	s_mov_b64 exec, s[50:51]
	global_load_dwordx4 v[20:23], v74, s[18:19] offset:1024 nt
	s_mov_b64 exec, s[52:53]
	global_load_dwordx4 v[24:27], v74, s[18:19] offset:2048 nt
	s_mov_b64 exec, s[54:55]
	global_load_dwordx4 v[28:31], v74, s[18:19] offset:3072 nt
	s_add_u32 s18, s18, 0x1000
	s_addc_u32 s19, s19, 0
	s_mov_b64 exec, s[56:57]
	global_load_dwordx4 v[32:35], v74, s[18:19] nt
	s_mov_b64 exec, s[58:59]
	global_load_dwordx4 v[36:39], v74, s[18:19] offset:1024 nt
	s_mov_b64 exec, s[60:61]
	global_load_dwordx4 v[40:43], v74, s[18:19] offset:2048 nt
	s_mov_b64 exec, s[62:63]
	global_load_dwordx4 v[44:47], v74, s[18:19] offset:3072 nt
	s_add_u32 s18, s18, 0x1000
	s_addc_u32 s19, s19, 0
	s_mov_b64 exec, s[64:65]
	global_load_dwordx4 v[48:51], v74, s[18:19] nt
	s_mov_b64 exec, s[66:67]
	global_load_dwordx4 v[52:55], v74, s[18:19] offset:1024 nt
	s_mov_b64 exec, s[68:69]
	global_load_dwordx4 v[56:59], v74, s[18:19] offset:2048 nt
	s_mov_b64 exec, s[70:71]
	global_load_dwordx4 v[60:63], v74, s[18:19] offset:3072 nt
	s_mov_b64 exec, -1
	v_mov_b32_e32 v96, 0
	v_mov_b32_e32 v97, 0
	v_mov_b32_e32 v98, 0
	v_mov_b32_e32 v99, 0
	v_mov_b32_e32 v100, 0
	v_mov_b32_e32 v101, 0
	v_mov_b32_e32 v102, 0
	v_mov_b32_e32 v103, 0
	s_waitcnt vmcnt(0)
	s_barrier
	s_mov_b64 exec, s[40:41]
	v_pk_fma_f32 v[96:97], v[80:81], v[0:1], v[96:97] op_sel_hi:[0,1,1]
	v_pk_fma_f32 v[98:99], v[80:81], v[2:3], v[98:99] op_sel_hi:[0,1,1]
	s_mov_b64 exec, s[42:43]
	v_pk_fma_f32 v[100:101], v[80:81], v[4:5], v[100:101] op_sel:[1,0,0]
	v_pk_fma_f32 v[102:103], v[80:81], v[6:7], v[102:103] op_sel:[1,0,0]
	s_mov_b64 exec, s[44:45]
	v_pk_fma_f32 v[96:97], v[82:83], v[8:9], v[96:97] op_sel_hi:[0,1,1]
	v_pk_fma_f32 v[98:99], v[82:83], v[10:11], v[98:99] op_sel_hi:[0,1,1]
	s_mov_b64 exec, s[46:47]
	v_pk_fma_f32 v[100:101], v[82:83], v[12:13], v[100:101] op_sel:[1,0,0]
	v_pk_fma_f32 v[102:103], v[82:83], v[14:15], v[102:103] op_sel:[1,0,0]
	s_mov_b64 exec, s[48:49]
	v_pk_fma_f32 v[96:97], v[84:85], v[16:17], v[96:97] op_sel_hi:[0,1,1]
	v_pk_fma_f32 v[98:99], v[84:85], v[18:19], v[98:99] op_sel_hi:[0,1,1]
	s_mov_b64 exec, s[50:51]
	v_pk_fma_f32 v[100:101], v[84:85], v[20:21], v[100:101] op_sel:[1,0,0]
	v_pk_fma_f32 v[102:103], v[84:85], v[22:23], v[102:103] op_sel:[1,0,0]
	s_mov_b64 exec, s[52:53]
	v_pk_fma_f32 v[96:97], v[86:87], v[24:25], v[96:97] op_sel_hi:[0,1,1]
	v_pk_fma_f32 v[98:99], v[86:87], v[26:27], v[98:99] op_sel_hi:[0,1,1]
	s_mov_b64 exec, s[54:55]
	v_pk_fma_f32 v[100:101], v[86:87], v[28:29], v[100:101] op_sel:[1,0,0]
	v_pk_fma_f32 v[102:103], v[86:87], v[30:31], v[102:103] op_sel:[1,0,0]
	s_mov_b64 exec, s[56:57]
	v_pk_fma_f32 v[96:97], v[88:89], v[32:33], v[96:97] op_sel_hi:[0,1,1]
	v_pk_fma_f32 v[98:99], v[88:89], v[34:35], v[98:99] op_sel_hi:[0,1,1]
	s_mov_b64 exec, s[58:59]
	v_pk_fma_f32 v[100:101], v[88:89], v[36:37], v[100:101] op_sel:[1,0,0]
	v_pk_fma_f32 v[102:103], v[88:89], v[38:39], v[102:103] op_sel:[1,0,0]
	s_mov_b64 exec, s[60:61]
	v_pk_fma_f32 v[96:97], v[90:91], v[40:41], v[96:97] op_sel_hi:[0,1,1]
	v_pk_fma_f32 v[98:99], v[90:91], v[42:43], v[98:99] op_sel_hi:[0,1,1]
	s_mov_b64 exec, s[62:63]
	v_pk_fma_f32 v[100:101], v[90:91], v[44:45], v[100:101] op_sel:[1,0,0]
	v_pk_fma_f32 v[102:103], v[90:91], v[46:47], v[102:103] op_sel:[1,0,0]
	s_mov_b64 exec, s[64:65]
	v_pk_fma_f32 v[96:97], v[92:93], v[48:49], v[96:97] op_sel_hi:[0,1,1]
	v_pk_fma_f32 v[98:99], v[92:93], v[50:51], v[98:99] op_sel_hi:[0,1,1]
	s_mov_b64 exec, s[66:67]
	v_pk_fma_f32 v[100:101], v[92:93], v[52:53], v[100:101] op_sel:[1,0,0]
	v_pk_fma_f32 v[102:103], v[92:93], v[54:55], v[102:103] op_sel:[1,0,0]
	s_mov_b64 exec, s[68:69]
	v_pk_fma_f32 v[96:97], v[94:95], v[56:57], v[96:97] op_sel_hi:[0,1,1]
	v_pk_fma_f32 v[98:99], v[94:95], v[58:59], v[98:99] op_sel_hi:[0,1,1]
	s_mov_b64 exec, s[70:71]
	v_pk_fma_f32 v[100:101], v[94:95], v[60:61], v[100:101] op_sel:[1,0,0]
	v_pk_fma_f32 v[102:103], v[94:95], v[62:63], v[102:103] op_sel:[1,0,0]
	s_mov_b64 exec, -1
	ds_read_b128 v[0:3], v74
	ds_read_b128 v[4:7], v74 offset:1024
	ds_read_b128 v[8:11], v74 offset:2048
	ds_read_b128 v[12:15], v74 offset:3072
	ds_read_b128 v[16:19], v74 offset:4096
	ds_read_b128 v[20:23], v74 offset:5120
	ds_read_b128 v[24:27], v74 offset:6144
	ds_read_b128 v[28:31], v74 offset:7168
	ds_read_b128 v[32:35], v74 offset:8192
	ds_read_b128 v[36:39], v74 offset:9216
	ds_read_b128 v[40:43], v74 offset:10240
	ds_read_b128 v[44:47], v74 offset:11264
	ds_read_b128 v[48:51], v74 offset:12288
	ds_read_b128 v[52:55], v74 offset:13312
	ds_read_b128 v[56:59], v74 offset:14336
	v_pk_add_f32 v[96:97], v[96:97], v[100:101]
	v_pk_add_f32 v[98:99], v[98:99], v[102:103]
	s_nop 1
	v_permlane16_swap_b32_e32 v96, v97
	v_permlane16_swap_b32_e32 v98, v99
	v_add_f32_e32 v96, v96, v97
	v_add_f32_e32 v98, v98, v99
	s_nop 1
	v_permlane32_swap_b32_e32 v96, v98
	v_add_f32_e32 v96, v96, v98
	v_add_f32_e32 v96, v96, v64
	s_waitcnt lgkmcnt(5)
	ds_read_b128 v[60:63], v74 offset:15360
	ds_write_b32 v78, v96
	ds_read2_b32 v[80:81], v79 offset0:0 offset1:4
	ds_read2_b32 v[82:83], v79 offset0:8 offset1:12
	ds_read2_b32 v[84:85], v79 offset0:16 offset1:20
	ds_read2_b32 v[86:87], v79 offset0:24 offset1:28
	ds_read2_b32 v[88:89], v79 offset0:32 offset1:36
	ds_read2_b32 v[90:91], v79 offset0:40 offset1:44
	ds_read2_b32 v[92:93], v79 offset0:48 offset1:52
	ds_read2_b32 v[94:95], v79 offset0:56 offset1:60
	v_lshlrev_b32_e32 v72, 3, v76
	v_lshl_or_b32 v72, v75, 2, v72
	v_cmp_gt_u32_e32 vcc, 2, v75
	s_waitcnt lgkmcnt(0)
	v_pk_mul_f32 v[96:97], v[80:81], v[0:1] op_sel_hi:[0,1]
	v_pk_mul_f32 v[98:99], v[80:81], v[2:3] op_sel_hi:[0,1]
	v_pk_mul_f32 v[100:101], v[80:81], v[4:5] op_sel:[1,0]
	v_pk_mul_f32 v[102:103], v[80:81], v[6:7] op_sel:[1,0]
	v_pk_fma_f32 v[96:97], v[82:83], v[8:9], v[96:97] op_sel_hi:[0,1,1]
	v_pk_fma_f32 v[98:99], v[82:83], v[10:11], v[98:99] op_sel_hi:[0,1,1]
	v_pk_fma_f32 v[100:101], v[82:83], v[12:13], v[100:101] op_sel:[1,0,0]
	v_pk_fma_f32 v[102:103], v[82:83], v[14:15], v[102:103] op_sel:[1,0,0]
	v_pk_fma_f32 v[96:97], v[84:85], v[16:17], v[96:97] op_sel_hi:[0,1,1]
	v_pk_fma_f32 v[98:99], v[84:85], v[18:19], v[98:99] op_sel_hi:[0,1,1]
	v_pk_fma_f32 v[100:101], v[84:85], v[20:21], v[100:101] op_sel:[1,0,0]
	v_pk_fma_f32 v[102:103], v[84:85], v[22:23], v[102:103] op_sel:[1,0,0]
	v_pk_fma_f32 v[96:97], v[86:87], v[24:25], v[96:97] op_sel_hi:[0,1,1]
	v_pk_fma_f32 v[98:99], v[86:87], v[26:27], v[98:99] op_sel_hi:[0,1,1]
	v_pk_fma_f32 v[100:101], v[86:87], v[28:29], v[100:101] op_sel:[1,0,0]
	v_pk_fma_f32 v[102:103], v[86:87], v[30:31], v[102:103] op_sel:[1,0,0]
	v_pk_fma_f32 v[96:97], v[88:89], v[32:33], v[96:97] op_sel_hi:[0,1,1]
	v_pk_fma_f32 v[98:99], v[88:89], v[34:35], v[98:99] op_sel_hi:[0,1,1]
	v_pk_fma_f32 v[100:101], v[88:89], v[36:37], v[100:101] op_sel:[1,0,0]
	v_pk_fma_f32 v[102:103], v[88:89], v[38:39], v[102:103] op_sel:[1,0,0]
	v_pk_fma_f32 v[96:97], v[90:91], v[40:41], v[96:97] op_sel_hi:[0,1,1]
	v_pk_fma_f32 v[98:99], v[90:91], v[42:43], v[98:99] op_sel_hi:[0,1,1]
	v_pk_fma_f32 v[100:101], v[90:91], v[44:45], v[100:101] op_sel:[1,0,0]
	v_pk_fma_f32 v[102:103], v[90:91], v[46:47], v[102:103] op_sel:[1,0,0]
	v_pk_fma_f32 v[96:97], v[92:93], v[48:49], v[96:97] op_sel_hi:[0,1,1]
	v_pk_fma_f32 v[98:99], v[92:93], v[50:51], v[98:99] op_sel_hi:[0,1,1]
	v_pk_fma_f32 v[100:101], v[92:93], v[52:53], v[100:101] op_sel:[1,0,0]
	v_pk_fma_f32 v[102:103], v[92:93], v[54:55], v[102:103] op_sel:[1,0,0]
	v_pk_fma_f32 v[96:97], v[94:95], v[56:57], v[96:97] op_sel_hi:[0,1,1]
	v_pk_fma_f32 v[98:99], v[94:95], v[58:59], v[98:99] op_sel_hi:[0,1,1]
	v_pk_fma_f32 v[100:101], v[94:95], v[60:61], v[100:101] op_sel:[1,0,0]
	v_pk_fma_f32 v[102:103], v[94:95], v[62:63], v[102:103] op_sel:[1,0,0]
	v_pk_add_f32 v[96:97], v[96:97], v[100:101]
	v_pk_add_f32 v[98:99], v[98:99], v[102:103]
	s_nop 1
	v_permlane16_swap_b32_e32 v96, v98
	v_permlane16_swap_b32_e32 v97, v99
	v_add_f32_e32 v96, v96, v98
	v_add_f32_e32 v97, v97, v99
	v_mov_b32_e32 v80, v96
	v_mov_b32_e32 v81, v97
	s_nop 1
	v_permlane32_swap_b32_e32 v96, v80
	v_permlane32_swap_b32_e32 v97, v81
	v_add_f32_e32 v96, v96, v80
	v_add_f32_e32 v97, v97, v81
	v_cvt_pk_f16_f32 v73, v96, v97
	s_and_saveexec_b64 s[4:5], vcc
	global_atomic_pk_add_f16 v72, v73, s[24:25]
	s_endpgm
	.p2align	8

_Z11edge_kernelILi64ELb0EEvPKfS1_PKDF16_PKiS5_S1_S1_S1_S1_S1_PDF16_:
	s_load_dwordx16 s[4:19], s[0:1], 0x10
	s_load_dwordx2 s[20:21], s[0:1], 0x50
	v_readfirstlane_b32 s3, v0
	v_bfe_u32 v75, v0, 4, 2
	v_and_b32_e32 v76, 15, v0
	v_and_b32_e32 v78, 63, v0
	s_lshr_b32 s3, s3, 6
	s_mul_i32 s26, s3, 0x1388
	s_add_i32 s2, s2, s26
	v_lshlrev_b32_e32 v74, 8, v75
	v_lshl_or_b32 v74, v76, 4, v74
	v_lshlrev_b32_e32 v79, 4, v78
	v_lshl_or_b32 v77, v76, 2, v75
	v_lshlrev_b32_e32 v77, 2, v77
	v_lshlrev_b32_e32 v78, 5, v75
	v_lshlrev_b32_e32 v73, 12, v75
	v_lshl_or_b32 v73, v76, 4, v73
	s_lshl_b32 s28, s2, 14
	s_lshl_b32 s29, s2, 14
	s_lshl_b32 s30, s2, 2
	s_lshl_b32 s31, s2, 8
	s_lshl_b32 s33, s3, 10
	s_lshl_b32 s34, s3, 8
	s_addk_i32 s34, 0x4000
	s_waitcnt lgkmcnt(0)
	s_add_u32 s6, s6, s30
	s_addc_u32 s7, s7, 0
	s_add_u32 s8, s8, s30
	s_addc_u32 s9, s9, 0
	s_load_dword s35, s[6:7], 0x0
	s_load_dword s36, s[8:9], 0x0
	s_add_u32 s10, s10, s28
	s_addc_u32 s11, s11, 0
	s_add_u32 s18, s18, s33
	s_addc_u32 s19, s19, 0
	s_add_u32 s14, s14, s29
	s_addc_u32 s15, s15, 0
	s_add_u32 s12, s12, s31
	s_addc_u32 s13, s13, 0
	s_add_u32 s16, s16, s31
	s_addc_u32 s17, s17, 0
	s_waitcnt lgkmcnt(0)
	s_lshl_b32 s36, s36, 7
	s_add_u32 s20, s20, s36
	s_addc_u32 s21, s21, 0
	s_lshl_b32 s37, s35, 7
	s_add_u32 s4, s4, s37
	s_addc_u32 s5, s5, 0
	global_load_dwordx4 v[64:67], v78, s[4:5] nt
	global_load_dwordx4 v[68:71], v78, s[4:5] offset:16 nt
	v_add_u32_e32 v78, s34, v77
	s_waitcnt vmcnt(0)
	v_cvt_f32_f16_e32 v80, v64
	v_cvt_f32_f16_sdwa v81, v64 dst_sel:DWORD dst_unused:UNUSED_PAD src0_sel:WORD_1
	v_cvt_f32_f16_e32 v82, v65
	v_cvt_f32_f16_sdwa v83, v65 dst_sel:DWORD dst_unused:UNUSED_PAD src0_sel:WORD_1
	v_cvt_f32_f16_e32 v84, v66
	v_cvt_f32_f16_sdwa v85, v66 dst_sel:DWORD dst_unused:UNUSED_PAD src0_sel:WORD_1
	v_cvt_f32_f16_e32 v86, v67
	v_cvt_f32_f16_sdwa v87, v67 dst_sel:DWORD dst_unused:UNUSED_PAD src0_sel:WORD_1
	v_cvt_f32_f16_e32 v88, v68
	v_cvt_f32_f16_sdwa v89, v68 dst_sel:DWORD dst_unused:UNUSED_PAD src0_sel:WORD_1
	v_cvt_f32_f16_e32 v90, v69
	v_cvt_f32_f16_sdwa v91, v69 dst_sel:DWORD dst_unused:UNUSED_PAD src0_sel:WORD_1
	v_cvt_f32_f16_e32 v92, v70
	v_cvt_f32_f16_sdwa v93, v70 dst_sel:DWORD dst_unused:UNUSED_PAD src0_sel:WORD_1
	v_cvt_f32_f16_e32 v94, v71
	v_cvt_f32_f16_sdwa v95, v71 dst_sel:DWORD dst_unused:UNUSED_PAD src0_sel:WORD_1
	v_max_f32_e32 v80, 0, v80
	v_max_f32_e32 v81, 0, v81
	v_max_f32_e32 v82, 0, v82
	v_max_f32_e32 v83, 0, v83
	v_max_f32_e32 v84, 0, v84
	v_max_f32_e32 v85, 0, v85
	v_max_f32_e32 v86, 0, v86
	v_max_f32_e32 v87, 0, v87
	v_max_f32_e32 v88, 0, v88
	v_max_f32_e32 v89, 0, v89
	v_max_f32_e32 v90, 0, v90
	v_max_f32_e32 v91, 0, v91
	v_max_f32_e32 v92, 0, v92
	v_max_f32_e32 v93, 0, v93
	v_max_f32_e32 v94, 0, v94
	v_max_f32_e32 v95, 0, v95
	v_cmp_neq_f32_e64 s[40:41], 0, v80
	v_cmp_neq_f32_e64 s[42:43], 0, v81
	v_cmp_neq_f32_e64 s[44:45], 0, v82
	v_cmp_neq_f32_e64 s[46:47], 0, v83
	v_cmp_neq_f32_e64 s[48:49], 0, v84
	v_cmp_neq_f32_e64 s[50:51], 0, v85
	v_cmp_neq_f32_e64 s[52:53], 0, v86
	v_cmp_neq_f32_e64 s[54:55], 0, v87
	v_cmp_neq_f32_e64 s[56:57], 0, v88
	v_cmp_neq_f32_e64 s[58:59], 0, v89
	v_cmp_neq_f32_e64 s[60:61], 0, v90
	v_cmp_neq_f32_e64 s[62:63], 0, v91
	v_cmp_neq_f32_e64 s[64:65], 0, v92
	v_cmp_neq_f32_e64 s[66:67], 0, v93
	v_cmp_neq_f32_e64 s[68:69], 0, v94
	v_cmp_neq_f32_e64 s[70:71], 0, v95
	v_lshlrev_b32_e32 v96, 12, v75
	v_lshl_or_b32 v96, v76, 4, v96
	s_mov_b64 exec, s[40:41]
	global_load_dwordx4 v[0:3], v96, s[10:11] nt
	s_mov_b64 exec, s[42:43]
	global_load_dwordx4 v[4:7], v96, s[10:11] offset:256 nt
	s_mov_b64 exec, s[44:45]
	global_load_dwordx4 v[8:11], v96, s[10:11] offset:512 nt
	s_mov_b64 exec, s[46:47]
	global_load_dwordx4 v[12:15], v96, s[10:11] offset:768 nt
	s_mov_b64 exec, s[48:49]
	global_load_dwordx4 v[16:19], v96, s[10:11] offset:1024 nt
	s_mov_b64 exec, s[50:51]
	global_load_dwordx4 v[20:23], v96, s[10:11] offset:1280 nt
	s_mov_b64 exec, s[52:53]
	global_load_dwordx4 v[24:27], v96, s[10:11] offset:1536 nt
	s_mov_b64 exec, s[54:55]
	global_load_dwordx4 v[28:31], v96, s[10:11] offset:1792 nt
	s_mov_b64 exec, s[56:57]
	global_load_dwordx4 v[32:35], v96, s[10:11] offset:2048 nt
	s_mov_b64 exec, s[58:59]
	global_load_dwordx4 v[36:39], v96, s[10:11] offset:2304 nt
	s_mov_b64 exec, s[60:61]
	global_load_dwordx4 v[40:43], v96, s[10:11] offset:2560 nt
	s_mov_b64 exec, s[62:63]
	global_load_dwordx4 v[44:47], v96, s[10:11] offset:2816 nt
	s_mov_b64 exec, s[64:65]
	global_load_dwordx4 v[48:51], v96, s[10:11] offset:3072 nt
	s_mov_b64 exec, s[66:67]
	global_load_dwordx4 v[52:55], v96, s[10:11] offset:3328 nt
	s_mov_b64 exec, s[68:69]
	global_load_dwordx4 v[56:59], v96, s[10:11] offset:3584 nt
	s_mov_b64 exec, s[70:71]
	global_load_dwordx4 v[60:63], v96, s[10:11] offset:3840 nt
	s_mov_b64 exec, -1
	s_mov_b32 m0, s33
	s_nop 0
	global_load_lds_dwordx4 v79, s[18:19]
	global_load_lds_dwordx4 v79, s[18:19] offset:2048
	s_add_u32 m0, m0, 0x1000
	s_add_u32 s18, s18, 0x1000
	s_addc_u32 s19, s19, 0
	global_load_lds_dwordx4 v79, s[18:19]
	global_load_lds_dwordx4 v79, s[18:19] offset:2048
	s_add_u32 m0, m0, 0x1000
	s_add_u32 s18, s18, 0x1000
	s_addc_u32 s19, s19, 0
	global_load_lds_dwordx4 v79, s[18:19]
	global_load_lds_dwordx4 v79, s[18:19] offset:2048
	s_add_u32 m0, m0, 0x1000
	s_add_u32 s18, s18, 0x1000
	s_addc_u32 s19, s19, 0
	global_load_lds_dwordx4 v79, s[18:19]
	global_load_lds_dwordx4 v79, s[18:19] offset:2048
	global_load_dword v72, v77, s[12:13] nt
	global_load_dword v73, v77, s[16:17] nt
	v_lshl_add_u32 v79, v75, 2, s34
	v_mov_b32_e32 v96, 0
	v_mov_b32_e32 v97, 0
	v_mov_b32_e32 v98, 0
	v_mov_b32_e32 v99, 0
	v_mov_b32_e32 v100, 0
	v_mov_b32_e32 v101, 0
	v_mov_b32_e32 v102, 0
	v_mov_b32_e32 v103, 0
	s_waitcnt vmcnt(0)
	s_barrier
	s_mov_b64 exec, s[40:41]
	v_pk_fma_f32 v[96:97], v[80:81], v[0:1], v[96:97] op_sel_hi:[0,1,1]
	v_pk_fma_f32 v[98:99], v[80:81], v[2:3], v[98:99] op_sel_hi:[0,1,1]
	s_mov_b64 exec, s[42:43]
	v_pk_fma_f32 v[100:101], v[80:81], v[4:5], v[100:101] op_sel:[1,0,0]
	v_pk_fma_f32 v[102:103], v[80:81], v[6:7], v[102:103] op_sel:[1,0,0]
	s_mov_b64 exec, s[44:45]
	v_pk_fma_f32 v[96:97], v[82:83], v[8:9], v[96:97] op_sel_hi:[0,1,1]
	v_pk_fma_f32 v[98:99], v[82:83], v[10:11], v[98:99] op_sel_hi:[0,1,1]
	s_mov_b64 exec, s[46:47]
	v_pk_fma_f32 v[100:101], v[82:83], v[12:13], v[100:101] op_sel:[1,0,0]
	v_pk_fma_f32 v[102:103], v[82:83], v[14:15], v[102:103] op_sel:[1,0,0]
	s_mov_b64 exec, s[48:49]
	v_pk_fma_f32 v[96:97], v[84:85], v[16:17], v[96:97] op_sel_hi:[0,1,1]
	v_pk_fma_f32 v[98:99], v[84:85], v[18:19], v[98:99] op_sel_hi:[0,1,1]
	s_mov_b64 exec, s[50:51]
	v_pk_fma_f32 v[100:101], v[84:85], v[20:21], v[100:101] op_sel:[1,0,0]
	v_pk_fma_f32 v[102:103], v[84:85], v[22:23], v[102:103] op_sel:[1,0,0]
	s_mov_b64 exec, s[52:53]
	v_pk_fma_f32 v[96:97], v[86:87], v[24:25], v[96:97] op_sel_hi:[0,1,1]
	v_pk_fma_f32 v[98:99], v[86:87], v[26:27], v[98:99] op_sel_hi:[0,1,1]
	s_mov_b64 exec, s[54:55]
	v_pk_fma_f32 v[100:101], v[86:87], v[28:29], v[100:101] op_sel:[1,0,0]
	v_pk_fma_f32 v[102:103], v[86:87], v[30:31], v[102:103] op_sel:[1,0,0]
	s_mov_b64 exec, s[56:57]
	v_pk_fma_f32 v[96:97], v[88:89], v[32:33], v[96:97] op_sel_hi:[0,1,1]
	v_pk_fma_f32 v[98:99], v[88:89], v[34:35], v[98:99] op_sel_hi:[0,1,1]
	s_mov_b64 exec, s[58:59]
	v_pk_fma_f32 v[100:101], v[88:89], v[36:37], v[100:101] op_sel:[1,0,0]
	v_pk_fma_f32 v[102:103], v[88:89], v[38:39], v[102:103] op_sel:[1,0,0]
	s_mov_b64 exec, s[60:61]
	v_pk_fma_f32 v[96:97], v[90:91], v[40:41], v[96:97] op_sel_hi:[0,1,1]
	v_pk_fma_f32 v[98:99], v[90:91], v[42:43], v[98:99] op_sel_hi:[0,1,1]
	s_mov_b64 exec, s[62:63]
	v_pk_fma_f32 v[100:101], v[90:91], v[44:45], v[100:101] op_sel:[1,0,0]
	v_pk_fma_f32 v[102:103], v[90:91], v[46:47], v[102:103] op_sel:[1,0,0]
	s_mov_b64 exec, s[64:65]
	v_pk_fma_f32 v[96:97], v[92:93], v[48:49], v[96:97] op_sel_hi:[0,1,1]
	v_pk_fma_f32 v[98:99], v[92:93], v[50:51], v[98:99] op_sel_hi:[0,1,1]
	s_mov_b64 exec, s[66:67]
	v_pk_fma_f32 v[100:101], v[92:93], v[52:53], v[100:101] op_sel:[1,0,0]
	v_pk_fma_f32 v[102:103], v[92:93], v[54:55], v[102:103] op_sel:[1,0,0]
	s_mov_b64 exec, s[68:69]
	v_pk_fma_f32 v[96:97], v[94:95], v[56:57], v[96:97] op_sel_hi:[0,1,1]
	v_pk_fma_f32 v[98:99], v[94:95], v[58:59], v[98:99] op_sel_hi:[0,1,1]
	s_mov_b64 exec, s[70:71]
	v_pk_fma_f32 v[100:101], v[94:95], v[60:61], v[100:101] op_sel:[1,0,0]
	v_pk_fma_f32 v[102:103], v[94:95], v[62:63], v[102:103] op_sel:[1,0,0]
	s_mov_b64 exec, -1
	v_pk_add_f32 v[96:97], v[96:97], v[100:101]
	v_pk_add_f32 v[98:99], v[98:99], v[102:103]
	s_nop 1
	v_permlane16_swap_b32_e32 v96, v97
	v_permlane16_swap_b32_e32 v98, v99
	v_add_f32_e32 v96, v96, v97
	v_add_f32_e32 v98, v98, v99
	s_nop 1
	v_permlane32_swap_b32_e32 v96, v98
	v_add_f32_e32 v96, v96, v98
	s_waitcnt vmcnt(1)
	v_add_f32_e32 v96, v96, v72
	v_max_f32_e32 v96, 0, v96
	ds_write_b32 v78, v96
	ds_read2_b32 v[80:81], v79 offset0:0 offset1:4
	ds_read2_b32 v[82:83], v79 offset0:8 offset1:12
	ds_read2_b32 v[84:85], v79 offset0:16 offset1:20
	ds_read2_b32 v[86:87], v79 offset0:24 offset1:28
	ds_read2_b32 v[88:89], v79 offset0:32 offset1:36
	ds_read2_b32 v[90:91], v79 offset0:40 offset1:44
	ds_read2_b32 v[92:93], v79 offset0:48 offset1:52
	ds_read2_b32 v[94:95], v79 offset0:56 offset1:60
	s_waitcnt lgkmcnt(0)
	v_cmp_neq_f32_e64 s[40:41], 0, v80
	v_cmp_neq_f32_e64 s[42:43], 0, v81
	v_cmp_neq_f32_e64 s[44:45], 0, v82
	v_cmp_neq_f32_e64 s[46:47], 0, v83
	v_cmp_neq_f32_e64 s[48:49], 0, v84
	v_cmp_neq_f32_e64 s[50:51], 0, v85
	v_cmp_neq_f32_e64 s[52:53], 0, v86
	v_cmp_neq_f32_e64 s[54:55], 0, v87
	v_cmp_neq_f32_e64 s[56:57], 0, v88
	v_cmp_neq_f32_e64 s[58:59], 0, v89
	v_cmp_neq_f32_e64 s[60:61], 0, v90
	v_cmp_neq_f32_e64 s[62:63], 0, v91
	v_cmp_neq_f32_e64 s[64:65], 0, v92
	v_cmp_neq_f32_e64 s[66:67], 0, v93
	v_cmp_neq_f32_e64 s[68:69], 0, v94
	v_cmp_neq_f32_e64 s[70:71], 0, v95
	s_mov_b64 exec, s[40:41]
	global_load_dwordx4 v[0:3], v74, s[14:15] nt
	s_mov_b64 exec, s[42:43]
	global_load_dwordx4 v[4:7], v74, s[14:15] offset:1024 nt
	s_mov_b64 exec, s[44:45]
	global_load_dwordx4 v[8:11], v74, s[14:15] offset:2048 nt
	s_mov_b64 exec, s[46:47]
	global_load_dwordx4 v[12:15], v74, s[14:15] offset:3072 nt
	s_add_u32 s14, s14, 0x1000
	s_addc_u32 s15, s15, 0
	s_mov_b64 exec, s[48:49]
	global_load_dwordx4 v[16:19], v74, s[14:15] nt
	s_mov_b64 exec, s[50:51]
	global_load_dwordx4 v[20:23], v74, s[14:15] offset:1024 nt
	s_mov_b64 exec, s[52:53]
	global_load_dwordx4 v[24:27], v74, s[14:15] offset:2048 nt
	s_mov_b64 exec, s[54:55]
	global_load_dwordx4 v[28:31], v74, s[14:15] offset:3072 nt
	s_add_u32 s14, s14, 0x1000
	s_addc_u32 s15, s15, 0
	s_mov_b64 exec, s[56:57]
	global_load_dwordx4 v[32:35], v74, s[14:15] nt
	s_mov_b64 exec, s[58:59]
	global_load_dwordx4 v[36:39], v74, s[14:15] offset:1024 nt
	s_mov_b64 exec, s[60:61]
	global_load_dwordx4 v[40:43], v74, s[14:15] offset:2048 nt
	s_mov_b64 exec, s[62:63]
	global_load_dwordx4 v[44:47], v74, s[14:15] offset:3072 nt
	s_add_u32 s14, s14, 0x1000
	s_addc_u32 s15, s15, 0
	s_mov_b64 exec, s[64:65]
	global_load_dwordx4 v[48:51], v74, s[14:15] nt
	s_mov_b64 exec, s[66:67]
	global_load_dwordx4 v[52:55], v74, s[14:15] offset:1024 nt
	s_mov_b64 exec, s[68:69]
	global_load_dwordx4 v[56:59], v74, s[14:15] offset:2048 nt
	s_mov_b64 exec, s[70:71]
	global_load_dwordx4 v[60:63], v74, s[14:15] offset:3072 nt
	s_mov_b64 exec, -1
	v_mov_b32_e32 v96, 0
	v_mov_b32_e32 v97, 0
	v_mov_b32_e32 v98, 0
	v_mov_b32_e32 v99, 0
	v_mov_b32_e32 v100, 0
	v_mov_b32_e32 v101, 0
	v_mov_b32_e32 v102, 0
	v_mov_b32_e32 v103, 0
	s_waitcnt vmcnt(0)
	s_mov_b64 exec, s[40:41]
	v_pk_fma_f32 v[96:97], v[80:81], v[0:1], v[96:97] op_sel_hi:[0,1,1]
	v_pk_fma_f32 v[98:99], v[80:81], v[2:3], v[98:99] op_sel_hi:[0,1,1]
	s_mov_b64 exec, s[42:43]
	v_pk_fma_f32 v[100:101], v[80:81], v[4:5], v[100:101] op_sel:[1,0,0]
	v_pk_fma_f32 v[102:103], v[80:81], v[6:7], v[102:103] op_sel:[1,0,0]
	s_mov_b64 exec, s[44:45]
	v_pk_fma_f32 v[96:97], v[82:83], v[8:9], v[96:97] op_sel_hi:[0,1,1]
	v_pk_fma_f32 v[98:99], v[82:83], v[10:11], v[98:99] op_sel_hi:[0,1,1]
	s_mov_b64 exec, s[46:47]
	v_pk_fma_f32 v[100:101], v[82:83], v[12:13], v[100:101] op_sel:[1,0,0]
	v_pk_fma_f32 v[102:103], v[82:83], v[14:15], v[102:103] op_sel:[1,0,0]
	s_mov_b64 exec, s[48:49]
	v_pk_fma_f32 v[96:97], v[84:85], v[16:17], v[96:97] op_sel_hi:[0,1,1]
	v_pk_fma_f32 v[98:99], v[84:85], v[18:19], v[98:99] op_sel_hi:[0,1,1]
	s_mov_b64 exec, s[50:51]
	v_pk_fma_f32 v[100:101], v[84:85], v[20:21], v[100:101] op_sel:[1,0,0]
	v_pk_fma_f32 v[102:103], v[84:85], v[22:23], v[102:103] op_sel:[1,0,0]
	s_mov_b64 exec, s[52:53]
	v_pk_fma_f32 v[96:97], v[86:87], v[24:25], v[96:97] op_sel_hi:[0,1,1]
	v_pk_fma_f32 v[98:99], v[86:87], v[26:27], v[98:99] op_sel_hi:[0,1,1]
	s_mov_b64 exec, s[54:55]
	v_pk_fma_f32 v[100:101], v[86:87], v[28:29], v[100:101] op_sel:[1,0,0]
	v_pk_fma_f32 v[102:103], v[86:87], v[30:31], v[102:103] op_sel:[1,0,0]
	s_mov_b64 exec, s[56:57]
	v_pk_fma_f32 v[96:97], v[88:89], v[32:33], v[96:97] op_sel_hi:[0,1,1]
	v_pk_fma_f32 v[98:99], v[88:89], v[34:35], v[98:99] op_sel_hi:[0,1,1]
	s_mov_b64 exec, s[58:59]
	v_pk_fma_f32 v[100:101], v[88:89], v[36:37], v[100:101] op_sel:[1,0,0]
	v_pk_fma_f32 v[102:103], v[88:89], v[38:39], v[102:103] op_sel:[1,0,0]
	s_mov_b64 exec, s[60:61]
	v_pk_fma_f32 v[96:97], v[90:91], v[40:41], v[96:97] op_sel_hi:[0,1,1]
	v_pk_fma_f32 v[98:99], v[90:91], v[42:43], v[98:99] op_sel_hi:[0,1,1]
	s_mov_b64 exec, s[62:63]
	v_pk_fma_f32 v[100:101], v[90:91], v[44:45], v[100:101] op_sel:[1,0,0]
	v_pk_fma_f32 v[102:103], v[90:91], v[46:47], v[102:103] op_sel:[1,0,0]
	s_mov_b64 exec, s[64:65]
	v_pk_fma_f32 v[96:97], v[92:93], v[48:49], v[96:97] op_sel_hi:[0,1,1]
	v_pk_fma_f32 v[98:99], v[92:93], v[50:51], v[98:99] op_sel_hi:[0,1,1]
	s_mov_b64 exec, s[66:67]
	v_pk_fma_f32 v[100:101], v[92:93], v[52:53], v[100:101] op_sel:[1,0,0]
	v_pk_fma_f32 v[102:103], v[92:93], v[54:55], v[102:103] op_sel:[1,0,0]
	s_mov_b64 exec, s[68:69]
	v_pk_fma_f32 v[96:97], v[94:95], v[56:57], v[96:97] op_sel_hi:[0,1,1]
	v_pk_fma_f32 v[98:99], v[94:95], v[58:59], v[98:99] op_sel_hi:[0,1,1]
	s_mov_b64 exec, s[70:71]
	v_pk_fma_f32 v[100:101], v[94:95], v[60:61], v[100:101] op_sel:[1,0,0]
	v_pk_fma_f32 v[102:103], v[94:95], v[62:63], v[102:103] op_sel:[1,0,0]
	s_mov_b64 exec, -1
	ds_read_b128 v[0:3], v74
	ds_read_b128 v[4:7], v74 offset:1024
	ds_read_b128 v[8:11], v74 offset:2048
	ds_read_b128 v[12:15], v74 offset:3072
	ds_read_b128 v[16:19], v74 offset:4096
	ds_read_b128 v[20:23], v74 offset:5120
	ds_read_b128 v[24:27], v74 offset:6144
	ds_read_b128 v[28:31], v74 offset:7168
	ds_read_b128 v[32:35], v74 offset:8192
	ds_read_b128 v[36:39], v74 offset:9216
	ds_read_b128 v[40:43], v74 offset:10240
	ds_read_b128 v[44:47], v74 offset:11264
	ds_read_b128 v[48:51], v74 offset:12288
	ds_read_b128 v[52:55], v74 offset:13312
	ds_read_b128 v[56:59], v74 offset:14336
	v_pk_add_f32 v[96:97], v[96:97], v[100:101]
	v_pk_add_f32 v[98:99], v[98:99], v[102:103]
	s_nop 1
	v_permlane16_swap_b32_e32 v96, v97
	v_permlane16_swap_b32_e32 v98, v99
	v_add_f32_e32 v96, v96, v97
	v_add_f32_e32 v98, v98, v99
	s_nop 1
	v_permlane32_swap_b32_e32 v96, v98
	v_add_f32_e32 v96, v96, v98
	v_add_f32_e32 v96, v96, v73
	s_waitcnt lgkmcnt(5)
	ds_read_b128 v[60:63], v74 offset:15360
	ds_write_b32 v78, v96
	ds_read2_b32 v[80:81], v79 offset0:0 offset1:4
	ds_read2_b32 v[82:83], v79 offset0:8 offset1:12
	ds_read2_b32 v[84:85], v79 offset0:16 offset1:20
	ds_read2_b32 v[86:87], v79 offset0:24 offset1:28
	ds_read2_b32 v[88:89], v79 offset0:32 offset1:36
	ds_read2_b32 v[90:91], v79 offset0:40 offset1:44
	ds_read2_b32 v[92:93], v79 offset0:48 offset1:52
	ds_read2_b32 v[94:95], v79 offset0:56 offset1:60
	v_lshlrev_b32_e32 v72, 3, v76
	v_lshl_or_b32 v72, v75, 2, v72
	v_cmp_gt_u32_e32 vcc, 2, v75
	s_waitcnt lgkmcnt(0)
	v_pk_mul_f32 v[96:97], v[80:81], v[0:1] op_sel_hi:[0,1]
	v_pk_mul_f32 v[98:99], v[80:81], v[2:3] op_sel_hi:[0,1]
	v_pk_mul_f32 v[100:101], v[80:81], v[4:5] op_sel:[1,0]
	v_pk_mul_f32 v[102:103], v[80:81], v[6:7] op_sel:[1,0]
	v_pk_fma_f32 v[96:97], v[82:83], v[8:9], v[96:97] op_sel_hi:[0,1,1]
	v_pk_fma_f32 v[98:99], v[82:83], v[10:11], v[98:99] op_sel_hi:[0,1,1]
	v_pk_fma_f32 v[100:101], v[82:83], v[12:13], v[100:101] op_sel:[1,0,0]
	v_pk_fma_f32 v[102:103], v[82:83], v[14:15], v[102:103] op_sel:[1,0,0]
	v_pk_fma_f32 v[96:97], v[84:85], v[16:17], v[96:97] op_sel_hi:[0,1,1]
	v_pk_fma_f32 v[98:99], v[84:85], v[18:19], v[98:99] op_sel_hi:[0,1,1]
	v_pk_fma_f32 v[100:101], v[84:85], v[20:21], v[100:101] op_sel:[1,0,0]
	v_pk_fma_f32 v[102:103], v[84:85], v[22:23], v[102:103] op_sel:[1,0,0]
	v_pk_fma_f32 v[96:97], v[86:87], v[24:25], v[96:97] op_sel_hi:[0,1,1]
	v_pk_fma_f32 v[98:99], v[86:87], v[26:27], v[98:99] op_sel_hi:[0,1,1]
	v_pk_fma_f32 v[100:101], v[86:87], v[28:29], v[100:101] op_sel:[1,0,0]
	v_pk_fma_f32 v[102:103], v[86:87], v[30:31], v[102:103] op_sel:[1,0,0]
	v_pk_fma_f32 v[96:97], v[88:89], v[32:33], v[96:97] op_sel_hi:[0,1,1]
	v_pk_fma_f32 v[98:99], v[88:89], v[34:35], v[98:99] op_sel_hi:[0,1,1]
	v_pk_fma_f32 v[100:101], v[88:89], v[36:37], v[100:101] op_sel:[1,0,0]
	v_pk_fma_f32 v[102:103], v[88:89], v[38:39], v[102:103] op_sel:[1,0,0]
	v_pk_fma_f32 v[96:97], v[90:91], v[40:41], v[96:97] op_sel_hi:[0,1,1]
	v_pk_fma_f32 v[98:99], v[90:91], v[42:43], v[98:99] op_sel_hi:[0,1,1]
	v_pk_fma_f32 v[100:101], v[90:91], v[44:45], v[100:101] op_sel:[1,0,0]
	v_pk_fma_f32 v[102:103], v[90:91], v[46:47], v[102:103] op_sel:[1,0,0]
	v_pk_fma_f32 v[96:97], v[92:93], v[48:49], v[96:97] op_sel_hi:[0,1,1]
	v_pk_fma_f32 v[98:99], v[92:93], v[50:51], v[98:99] op_sel_hi:[0,1,1]
	v_pk_fma_f32 v[100:101], v[92:93], v[52:53], v[100:101] op_sel:[1,0,0]
	v_pk_fma_f32 v[102:103], v[92:93], v[54:55], v[102:103] op_sel:[1,0,0]
	v_pk_fma_f32 v[96:97], v[94:95], v[56:57], v[96:97] op_sel_hi:[0,1,1]
	v_pk_fma_f32 v[98:99], v[94:95], v[58:59], v[98:99] op_sel_hi:[0,1,1]
	v_pk_fma_f32 v[100:101], v[94:95], v[60:61], v[100:101] op_sel:[1,0,0]
	v_pk_fma_f32 v[102:103], v[94:95], v[62:63], v[102:103] op_sel:[1,0,0]
	v_pk_add_f32 v[96:97], v[96:97], v[100:101]
	v_pk_add_f32 v[98:99], v[98:99], v[102:103]
	s_nop 1
	v_permlane16_swap_b32_e32 v96, v98
	v_permlane16_swap_b32_e32 v97, v99
	v_add_f32_e32 v96, v96, v98
	v_add_f32_e32 v97, v97, v99
	v_mov_b32_e32 v80, v96
	v_mov_b32_e32 v81, v97
	s_nop 1
	v_permlane32_swap_b32_e32 v96, v80
	v_permlane32_swap_b32_e32 v97, v81
	v_add_f32_e32 v96, v96, v80
	v_add_f32_e32 v97, v97, v81
	v_cvt_pk_f16_f32 v73, v96, v97
	s_and_saveexec_b64 s[4:5], vcc
	global_atomic_pk_add_f16 v72, v73, s[20:21]
	s_endpgm
	.p2align	8
